# output GEMM column-tile order rotated by (panel & 3) as well
# baseline (speedup 1.0000x reference)
.LBB0_252:
	v_readlane_b32 s0, v253, 0
	v_readlane_b32 s1, v253, 1
	s_add_u32 s0, s0, 0x37a00000
	s_addc_u32 s1, s1, 0
	v_writelane_b32 v254, s0, 32
	s_mov_b32 s97, 0
	s_mov_b32 s92, 1
	v_writelane_b32 v254, s1, 33
	v_readlane_b32 s0, v253, 15
	v_readlane_b32 s1, v253, 16
	v_readlane_b32 s16, v254, 42
	s_and_b64 s[18:19], s[0:1], s[14:15]
	v_readlane_b32 s17, v254, 43
	s_and_b64 s[0:1], s[16:17], s[18:19]
	s_xor_b64 s[0:1], s[0:1], -1
	v_writelane_b32 v254, s0, 44
	s_movk_i32 s68, 0x1800
	v_mov_b32_e32 v97, 0
	v_writelane_b32 v254, s1, 45
	v_readlane_b32 s0, v253, 34
	v_readlane_b32 s2, v253, 36
	v_readlane_b32 s1, v253, 35
	v_readlane_b32 s3, v253, 37
	s_add_u32 s0, s2, 0x2000
	s_addc_u32 s1, s3, 0
	v_writelane_b32 v254, s0, 46
	v_readlane_b32 s7, v253, 41
	s_ashr_i32 s7, s50, 31
	v_writelane_b32 v254, s1, 47
	v_readlane_b32 s0, v253, 9
	s_lshl_b32 s0, s0, 6
	s_sub_i32 s65, 0, s0
	s_lshr_b32 s0, s7, 29
	v_readlane_b32 s8, v253, 42
	s_add_i32 s0, s50, s0
	v_readlane_b32 s9, v253, 43
	v_readlane_b32 s10, v253, 44
	s_ashr_i32 s8, s0, 3
	s_and_b32 s0, s0, -8
	s_sub_i32 s9, s50, s0
	s_ashr_i32 s10, s61, 31
	s_and_b64 s[0:1], s[16:17], exec
	s_cselect_b32 s0, 1, s61
	v_readlane_b32 s2, v253, 8
	v_writelane_b32 v254, s0, 48
	s_and_b32 s0, s2, 0xffffffe0
	s_bfe_u32 s1, s2, 0x20003
	v_readlane_b32 s4, v253, 38
	s_or_b32 s0, s1, s0
	v_readlane_b32 s5, v253, 39
	s_sub_i32 s4, s61, s2
	v_writelane_b32 v254, s0, 49
	s_and_b32 s0, s2, 7
	v_readlane_b32 s6, v253, 40
	v_readlane_b32 s11, v253, 45
	v_readlane_b32 s12, v253, 46
	v_readlane_b32 s13, v253, 47
	v_readlane_b32 s14, v253, 48
	v_readlane_b32 s15, v253, 49
	s_add_i32 s5, s4, 0xff
	v_writelane_b32 v253, s0, 15
	s_xor_b32 s0, s0, 15
	s_cmpk_gt_i32 s50, 0x3ff
	v_writelane_b32 v254, s0, 10
	s_cselect_b64 s[0:1], -1, 0
	s_and_b32 s2, s50, 7
	v_writelane_b32 v254, s2, 50
	s_ashr_i32 s11, s50, 3
	s_lshr_b32 s2, s7, 26
	s_add_i32 s2, s11, s2
	s_ashr_i32 s3, s2, 6
	s_andn2_b32 s2, s2, 63
	s_lshl_b32 s6, s9, 7
	s_lshl_b32 s3, s3, 3
	s_sub_i32 s12, s11, s2
	v_writelane_b32 v254, s3, 51
	s_and_b64 s[2:3], s[18:19], exec
	s_cselect_b32 s69, 64, 0
	s_sub_i32 s2, 0, s64
	v_writelane_b32 v254, s2, 52
	v_writelane_b32 v254, s18, 28
	s_xor_b64 s[2:3], s[18:19], -1
	s_movk_i32 s75, 0x1000
	v_writelane_b32 v254, s19, 29
	v_writelane_b32 v254, s2, 40
	s_movk_i32 s66, 0x2000
	s_movk_i32 s67, 0x7fff
	v_writelane_b32 v254, s3, 41
	s_lshr_b32 s2, s7, 27
	s_add_i32 s2, s11, s2
	s_ashr_i32 s3, s2, 5
	s_lshl_b32 s3, s3, 3
	v_writelane_b32 v254, s3, 53
	s_andn2_b32 s2, s2, 31
	v_writelane_b32 v254, s11, 19
	s_sub_i32 s11, s11, s2
	v_readlane_b32 s2, v253, 11
	s_cmp_lt_u32 s2, 64
	s_cselect_b64 s[2:3], -1, 0
	v_writelane_b32 v254, s2, 54
	s_or_b64 s[0:1], s[16:17], s[0:1]
	v_mov_b32_e32 v220, 0x358637bd
	v_writelane_b32 v254, s3, 55
	s_and_b32 s2, s7, s61
	v_writelane_b32 v254, s7, 39
	s_add_i32 s2, s2, s50
	v_writelane_b32 v254, s2, 56
	s_ashr_i32 s2, s2, 1
	v_writelane_b32 v254, s2, 57
	s_ashr_i32 s2, s2, 31
	v_writelane_b32 v254, s2, 58
	s_lshr_b32 s2, s9, 31
	v_writelane_b32 v254, s2, 59
	s_cmp_lt_i32 s9, 0
	s_mul_i32 s2, s9, 0x81
	s_cselect_b32 s2, s2, s6
	s_add_i32 s2, s2, s8
	s_ashr_i32 s3, s2, 31
	s_lshr_b32 s3, s3, 27
	s_add_i32 s3, s2, s3
	s_ashr_i32 s6, s3, 5
	s_and_b32 s3, s3, 0xffe0
	s_sub_i32 s2, s2, s3
	s_bfe_i32 s3, s2, 0x80000
	s_bfe_u32 s3, s3, 0x3000c
	s_add_i32 s3, s2, s3
	s_bfe_i32 s7, s3, 0x80000
	s_and_b32 s3, s3, 0xf8
	s_sub_i32 s2, s2, s3
	s_lshl_b32 s6, s6, 3
	s_sext_i32_i16 s7, s7
	s_sext_i32_i8 s2, s2
	s_add_i32 s6, s6, s2
	s_ashr_i32 s7, s7, 3
	v_writelane_b32 v254, s9, 60
	s_and_b32 s98, s93, 3
	s_and_b64 s[2:3], s[0:1], exec
	v_writelane_b32 v254, s8, 61
	s_cselect_b32 s8, s98, s7
	s_and_b64 s[2:3], s[16:17], exec
	s_cselect_b32 s2, s93, s6
	s_abs_i32 s6, s61
	s_waitcnt vmcnt(0)
	v_cvt_f32_u32_e32 v0, s6
	s_xor_b64 s[0:1], s[0:1], -1
	s_or_b64 s[0:1], s[16:17], s[0:1]
	v_writelane_b32 v254, s0, 62
	v_rcp_iflag_f32_e32 v0, v0
	v_writelane_b32 v255, s2, 0
	v_writelane_b32 v254, s1, 63
	s_lshl_b32 s0, s2, 8
	v_mul_f32_e32 v0, 0x4f7ffffe, v0
	v_cvt_u32_f32_e32 v0, v0
	v_writelane_b32 v255, s0, 1
	s_mov_b32 s0, s8
	s_ashr_i32 s9, s8, 31
	v_writelane_b32 v255, s0, 2
	s_sub_i32 s2, 0, s6
	v_readfirstlane_b32 s3, v0
	v_writelane_b32 v255, s1, 3
	s_lshl_b64 s[0:1], s[8:9], 18
	v_writelane_b32 v255, s0, 4
	s_mul_i32 s2, s2, s3
	s_mul_hi_u32 s2, s3, s2
	v_writelane_b32 v255, s1, 5
	s_sub_i32 s1, 0xffffff01, s4
	s_max_i32 s1, s5, s1
	s_add_i32 s2, s3, s2
	v_writelane_b32 v255, s2, 6
	s_mul_hi_u32 s2, s1, s2
	s_mul_i32 s3, s2, s6
	s_ashr_i32 s0, s5, 31
	s_sub_i32 s1, s1, s3
	s_xor_b32 s0, s0, s10
	s_add_i32 s3, s2, 1
	s_sub_i32 s4, s1, s6
	s_cmp_ge_u32 s1, s6
	s_cselect_b32 s2, s3, s2
	s_cselect_b32 s1, s4, s1
	s_add_i32 s3, s2, 1
	s_cmp_ge_u32 s1, s6
	s_cselect_b32 s1, s3, s2
	s_xor_b32 s1, s1, s0
	s_sub_i32 s0, s1, s0
	v_writelane_b32 v255, s6, 7
	s_lshl_b32 s0, s0, 4
	v_writelane_b32 v255, s0, 8
	s_ashr_i32 s0, s12, 31
	v_writelane_b32 v255, s0, 9
	v_writelane_b32 v255, s12, 10
	s_abs_i32 s0, s12
	v_writelane_b32 v255, s0, 11
	s_ashr_i32 s0, s11, 31
	v_writelane_b32 v255, s0, 12
	s_abs_i32 s0, s11
	v_writelane_b32 v255, s11, 13
	s_bitcmp1_b32 s61, 0
	v_writelane_b32 v254, s10, 38
	v_writelane_b32 v255, s0, 14
	s_cselect_b64 s[0:1], -1, 0
	v_writelane_b32 v254, s0, 13
	s_mov_b32 s95, 0xf800000
	v_mbcnt_lo_u32_b32 v0, -1, 0
	v_writelane_b32 v254, s1, 14
	s_add_i32 s0, 0, 0x15200
	v_writelane_b32 v253, s0, 11
	s_add_i32 s0, 0, 0x12200
	v_writelane_b32 v255, s0, 15
	s_add_i32 s0, 0, 0x16300
	v_writelane_b32 v255, s0, 16
	s_add_i32 s0, 0, 0x16700
	v_writelane_b32 v255, s0, 17
	s_add_i32 s0, 0, 0x16280
	v_writelane_b32 v255, s0, 18
	s_add_i32 s0, 0, 0x201c0
	v_writelane_b32 v254, s0, 30
	s_add_i32 s0, 0, 0x20250
	v_writelane_b32 v255, s0, 19
	s_add_i32 s0, 0, 0x201d0
	v_writelane_b32 v255, s0, 20
	s_add_i32 s0, 0, 0x20260
	v_writelane_b32 v255, s0, 21
	s_add_i32 s0, 0, 0x201e0
	v_writelane_b32 v255, s0, 22
	s_add_i32 s0, 0, 0x20270
	v_writelane_b32 v255, s0, 23
	s_add_i32 s0, 0, 0x201f0
	v_writelane_b32 v255, s0, 24
	s_add_i32 s0, 0, 0x20280
	v_writelane_b32 v255, s0, 25
	s_add_i32 s0, 0, 0x20200
	v_writelane_b32 v255, s0, 26
	s_add_i32 s0, 0, 0x20290
	v_writelane_b32 v255, s0, 27
	s_add_i32 s0, 0, 0x20210
	v_writelane_b32 v255, s0, 28
	s_add_i32 s0, 0, 0x20220
	v_writelane_b32 v254, s0, 15
	s_add_i32 s0, 0, 0x201c4
	v_writelane_b32 v255, s0, 29
	s_add_i32 s0, 0, 0x201c8
	v_writelane_b32 v255, s0, 30
	s_add_i32 s0, 0, 0x201cc
	v_writelane_b32 v255, s0, 31
	s_add_i32 s0, 0, 0x201d4
	v_writelane_b32 v255, s0, 32
	s_add_i32 s0, 0, 0x201d8
	v_writelane_b32 v255, s0, 33
	s_add_i32 s0, 0, 0x201dc
	v_writelane_b32 v255, s0, 34
	s_add_i32 s0, 0, 0x201e4
	v_writelane_b32 v255, s0, 35
	s_add_i32 s0, 0, 0x201e8
	v_writelane_b32 v255, s0, 36
	s_add_i32 s0, 0, 0x201ec
	v_writelane_b32 v255, s0, 37
	s_add_i32 s0, 0, 0x201f4
	v_writelane_b32 v255, s0, 38
	s_add_i32 s0, 0, 0x201f8
	v_writelane_b32 v255, s0, 39
	s_add_i32 s0, 0, 0x201fc
	v_writelane_b32 v255, s0, 40
	s_add_i32 s0, 0, 0x20204
	v_writelane_b32 v255, s0, 41
	s_add_i32 s0, 0, 0x20208
	v_writelane_b32 v255, s0, 42
	s_add_i32 s0, 0, 0x2020c
	v_writelane_b32 v255, s0, 43
	s_add_i32 s0, 0, 0x20214
	v_writelane_b32 v255, s0, 44
	s_add_i32 s0, 0, 0x20218
	v_writelane_b32 v255, s0, 45
	s_add_i32 s0, 0, 0x2021c
	v_writelane_b32 v255, s0, 46
	s_add_i32 s0, 0, 0x201a0
	v_writelane_b32 v254, s0, 8
	v_writelane_b32 v254, s42, 34
	v_mov_b32_e32 v221, 0x260
	s_mov_b32 s82, 0xc3e00000
	v_writelane_b32 v254, s43, 35
	v_writelane_b32 v254, s50, 31
	v_mov_b32_e32 v222, 0x3ca908c9
	s_mov_b32 s83, 0x3f2aaaab
	v_mov_b32_e32 v223, 0x3ecc95a3
	v_mov_b32_e32 v225, 0x7f7f7f7f
	v_mov_b32_e32 v226, 0x7a7a7a7a
	v_mov_b32_e32 v228, 0x7d7d7d7d
	v_mbcnt_hi_u32_b32 v227, -1, v0
	v_mov_b32_e32 v229, 0x43e00000
	v_mov_b32_e32 v230, 0x7f800000
	v_mov_b32_e32 v198, 0x3f317218
	v_mov_b32_e32 v231, 0x7fc00000
	v_mov_b32_e32 v232, 0xff800000
	v_mov_b32_e32 v233, 0x300
	v_mov_b32_e32 v234, 0x1800
	v_mov_b64_e32 v[200:201], 0x1e8481
	s_add_i32 s76, 0, 0x10800
	s_add_i32 s77, 0, 0x14800
	s_add_i32 s94, 0, 0x18800
	s_add_i32 s33, 0, 0x1c800
	s_mov_b32 s84, 0x5040100
	s_mov_b32 s85, 0xffff
	s_mov_b64 s[86:87], 0x1000
	s_mov_b32 s74, 0xbfb8aa3b
	s_mov_b64 s[62:63], 0x40000
	s_mov_b32 s4, s97
	s_mov_b32 s88, 0x3f803f80
	v_writelane_b32 v255, s65, 47
	v_writelane_b32 v254, s93, 7
	s_branch .LBB0_255

.LBB0_979:
	s_andn2_b64 vcc, exec, s[0:1]
	s_cbranch_vccnz .LBB0_983
	s_cmp_gt_u32 s14, 2
	s_mov_b64 s[8:9], 0
	s_cbranch_scc1 .LBB0_982
	s_mov_b64 s[8:9], -1
	s_mov_b32 s13, s93
	s_and_b32 s12, s93, 3
	s_add_i32 s12, s12, s46
	s_and_b32 s12, s12, 3
